# speedup vs baseline: 1.0171x; 1.0171x over previous
.Lp_main:
	s_load_dwordx2 s[10:11], s[0:1], 0x0
	s_load_dwordx4 s[12:15], s[0:1], 0x10
	s_load_dwordx2 s[16:17], s[0:1], 0x20
	s_load_dwordx4 s[20:23], s[0:1], 0x28
	v_readfirstlane_b32 s3, v0
	v_and_b32_e32 v154, 63, v0
	v_lshrrev_b32_e32 v155, 5, v154
	v_lshlrev_b32_e32 v156, 4, v0
	v_lshlrev_b32_e32 v157, 4, v154
	v_lshlrev_b32_e32 v158, 8, v1
	v_lshl_add_u32 v158, v155, 5, v158
	v_lshlrev_b32_e32 v159, 4, v155
	v_lshrrev_b32_e32 v160, 3, v0
	v_lshlrev_b32_e32 v160, 12, v160
	v_and_b32_e32 v161, 7, v0
	v_lshl_add_u32 v160, v161, 4, v160
	s_lshr_b32 s41, s2, 3
	s_and_b32 s42, s2, 7
	s_lshl_b32 s24, s42, 2
	s_bfe_u32 s25, s2, 0x20003
	s_add_u32 s24, s24, s25
	s_lshr_b32 s25, s2, 5
	s_lshr_b32 s26, s3, 6
	s_lshl_b32 s27, s25, 2
	s_add_u32 s27, s27, s26
	s_mov_b32 s4, 0x4038aa3b
	s_mov_b32 s5, s4
	s_lshl_b32 s40, s26, 6
	s_waitcnt lgkmcnt(0)
	s_lshl_b32 s28, s24, 15
	s_add_u32 s28, s28, 0x1000
	s_add_u32 s10, s10, s28
	s_addc_u32 s11, s11, 0
	s_lshl_b32 s34, s41, 17
	s_lshl_b32 s35, s42, 9
	s_add_u32 s34, s34, s35
	s_add_u32 s34, s14, s34
	s_addc_u32 s35, s15, 0
	s_lshl_b32 s28, s27, 13
	s_add_u32 s28, s8, s28
	s_addc_u32 s29, s9, 0
	s_lshl_b32 s30, s27, 7
	s_add_u32 s30, s12, s30
	s_addc_u32 s31, s13, 0
	global_load_dwordx4 v[2:5], v156, s[10:11] offset:-4096
	global_load_dwordx4 v[6:9], v156, s[10:11] offset:0
	s_add_u32 s10, s10, 0x2000
	s_addc_u32 s11, s11, 0
	global_load_dwordx4 v[10:13], v156, s[10:11] offset:-4096
	global_load_dwordx4 v[14:17], v156, s[10:11] offset:0
	s_add_u32 s10, s10, 0x2000
	s_addc_u32 s11, s11, 0
	global_load_dwordx4 v[18:21], v156, s[10:11] offset:-4096
	global_load_dwordx4 v[22:25], v156, s[10:11] offset:0
	s_add_u32 s10, s10, 0x2000
	s_addc_u32 s11, s11, 0
	global_load_dwordx4 v[26:29], v156, s[10:11] offset:-4096
	global_load_dwordx4 v[30:33], v156, s[10:11] offset:0
	global_load_dwordx4 v[130:133], v160, s[34:35] offset:0
	global_load_dwordx4 v[134:137], v160, s[34:35] offset:128
	global_load_dwordx4 v[138:141], v160, s[34:35] offset:256
	global_load_dwordx4 v[142:145], v160, s[34:35] offset:384
	global_load_dwordx4 v[34:37], v158, s[28:29] offset:0
	global_load_dwordx4 v[38:41], v158, s[28:29] offset:16
	global_load_dwordx4 v[42:45], v158, s[28:29] offset:64
	global_load_dwordx4 v[46:49], v158, s[28:29] offset:80
	global_load_dwordx4 v[50:53], v158, s[28:29] offset:128
	global_load_dwordx4 v[54:57], v158, s[28:29] offset:144
	global_load_dwordx4 v[58:61], v158, s[28:29] offset:192
	global_load_dwordx4 v[62:65], v158, s[28:29] offset:208
	global_load_dwordx4 v[66:69], v159, s[30:31] offset:0
	global_load_dwordx4 v[70:73], v159, s[30:31] offset:32
	global_load_dwordx4 v[74:77], v159, s[30:31] offset:64
	global_load_dwordx4 v[78:81], v159, s[30:31] offset:96
	s_getpc_b64 s[44:45]
	v_lshlrev_b32_e32 v162, 7, v154
	global_load_dword v162, v162, s[44:45]
	v_bfe_u32 v163, v0, 1, 3
	v_mul_u32_u24_e32 v163, 0x210, v163
	v_lshrrev_b32_e32 v164, 4, v0
	v_lshl_add_u32 v163, v164, 4, v163
	v_and_b32_e32 v164, 1, v0
	v_lshl_add_u32 v163, v164, 3, v163
	v_lshrrev_b32_e32 v164, 3, v0
	v_mul_u32_u24_e32 v164, 0x110, v164
	v_lshl_add_u32 v164, v161, 3, v164
	v_add_u32_e32 v164, 0x4200, v164
	v_mul_u32_u24_e32 v165, 0x210, v155
	v_lshl_add_u32 v165, v1, 4, v165
	v_mul_u32_u24_e32 v166, 0x110, v1
	v_lshl_add_u32 v166, v155, 4, v166
	v_add_u32_e32 v166, s40, v166
	v_add_u32_e32 v166, 0x4200, v166
	v_mul_u32_u24_e32 v167, 0x880, v155
	v_lshl_add_u32 v167, v1, 1, v167
	v_add_u32_e32 v167, s40, v167
	v_add_u32_e32 v167, 0x4200, v167
	s_lshl_b32 s32, s24, 18
	s_lshl_b32 s33, s27, 11
	s_add_u32 s32, s32, s33
	s_add_u32 s32, s16, s32
	s_addc_u32 s33, s17, 0
	s_lshl_b32 s36, s41, 16
	s_lshl_b32 s37, s42, 13
	s_add_u32 s36, s36, s37
	s_lshl_b32 s37, s26, 11
	s_add_u32 s36, s36, s37
	s_add_u32 s36, s20, s36
	s_addc_u32 s37, s21, 0
	s_lshl_b32 s38, s42, 18
	s_lshl_b32 s39, s26, 16
	s_add_u32 s38, s38, s39
	s_lshl_b32 s39, s41, 11
	s_add_u32 s38, s38, s39
	s_add_u32 s38, s22, s38
	s_addc_u32 s39, s23, 0
	s_waitcnt vmcnt(24)
	v_cvt_pk_f16_f32 v2, v2, v3
	v_cvt_pk_f16_f32 v3, v4, v5
	ds_write_b64 v163, v[2:3] offset:0
	s_waitcnt vmcnt(23)
	v_cvt_pk_f16_f32 v6, v6, v7
	v_cvt_pk_f16_f32 v7, v8, v9
	ds_write_b64 v163, v[6:7] offset:256
	s_waitcnt vmcnt(22)
	v_cvt_pk_f16_f32 v10, v10, v11
	v_cvt_pk_f16_f32 v11, v12, v13
	ds_write_b64 v163, v[10:11] offset:4224
	s_waitcnt vmcnt(21)
	v_cvt_pk_f16_f32 v14, v14, v15
	v_cvt_pk_f16_f32 v15, v16, v17
	ds_write_b64 v163, v[14:15] offset:4480
	s_waitcnt vmcnt(20)
	v_cvt_pk_f16_f32 v18, v18, v19
	v_cvt_pk_f16_f32 v19, v20, v21
	ds_write_b64 v163, v[18:19] offset:8448
	s_waitcnt vmcnt(19)
	v_cvt_pk_f16_f32 v22, v22, v23
	v_cvt_pk_f16_f32 v23, v24, v25
	ds_write_b64 v163, v[22:23] offset:8704
	s_waitcnt vmcnt(18)
	v_cvt_pk_f16_f32 v26, v26, v27
	v_cvt_pk_f16_f32 v27, v28, v29
	ds_write_b64 v163, v[26:27] offset:12672
	s_waitcnt vmcnt(17)
	v_cvt_pk_f16_f32 v30, v30, v31
	v_cvt_pk_f16_f32 v31, v32, v33
	ds_write_b64 v163, v[30:31] offset:12928
	s_waitcnt vmcnt(16)
	v_cvt_pk_f16_f32 v130, v130, v131
	v_cvt_pk_f16_f32 v131, v132, v133
	ds_write_b64 v164, v[130:131] offset:0
	s_waitcnt vmcnt(15)
	v_cvt_pk_f16_f32 v134, v134, v135
	v_cvt_pk_f16_f32 v135, v136, v137
	ds_write_b64 v164, v[134:135] offset:64
	s_waitcnt vmcnt(14)
	v_cvt_pk_f16_f32 v138, v138, v139
	v_cvt_pk_f16_f32 v139, v140, v141
	ds_write_b64 v164, v[138:139] offset:128
	s_waitcnt vmcnt(13)
	v_cvt_pk_f16_f32 v142, v142, v143
	v_cvt_pk_f16_f32 v143, v144, v145
	ds_write_b64 v164, v[142:143] offset:192
	s_waitcnt lgkmcnt(0)
	s_barrier
	ds_read_b128 v[130:133], v166
	ds_read_b128 v[134:137], v166 offset:32
	ds_read_u16 v138, v167 offset:0
	ds_read_u16 v139, v167 offset:272
	ds_read_u16 v140, v167 offset:544
	ds_read_u16 v141, v167 offset:816
	ds_read_u16 v142, v167 offset:1088
	ds_read_u16 v143, v167 offset:1360
	ds_read_u16 v144, v167 offset:1632
	ds_read_u16 v145, v167 offset:1904
	s_waitcnt vmcnt(5)
	v_cvt_pk_f16_f32 v82, v34, v35
	v_cvt_pk_f16_f32 v83, v36, v37
	v_cvt_pk_f16_f32 v84, v38, v39
	v_cvt_pk_f16_f32 v85, v40, v41
	v_cvt_pk_f16_f32 v86, v42, v43
	v_cvt_pk_f16_f32 v87, v44, v45
	v_cvt_pk_f16_f32 v88, v46, v47
	v_cvt_pk_f16_f32 v89, v48, v49
	v_cvt_pk_f16_f32 v90, v50, v51
	v_cvt_pk_f16_f32 v91, v52, v53
	v_cvt_pk_f16_f32 v92, v54, v55
	v_cvt_pk_f16_f32 v93, v56, v57
	v_cvt_pk_f16_f32 v94, v58, v59
	v_cvt_pk_f16_f32 v95, v60, v61
	v_cvt_pk_f16_f32 v96, v62, v63
	v_cvt_pk_f16_f32 v97, v64, v65
	s_waitcnt vmcnt(1)
	v_pk_mul_f32 v[66:67], v[66:67], s[4:5] op_sel_hi:[1,0]
	v_pk_mul_f32 v[68:69], v[68:69], s[4:5] op_sel_hi:[1,0]
	v_pk_mul_f32 v[70:71], v[70:71], s[4:5] op_sel_hi:[1,0]
	v_pk_mul_f32 v[72:73], v[72:73], s[4:5] op_sel_hi:[1,0]
	v_pk_mul_f32 v[74:75], v[74:75], s[4:5] op_sel_hi:[1,0]
	v_pk_mul_f32 v[76:77], v[76:77], s[4:5] op_sel_hi:[1,0]
	v_pk_mul_f32 v[78:79], v[78:79], s[4:5] op_sel_hi:[1,0]
	v_pk_mul_f32 v[80:81], v[80:81], s[4:5] op_sel_hi:[1,0]
	s_waitcnt lgkmcnt(8)
	global_store_dwordx4 v157, v[130:133], s[36:37] sc1
	global_store_dwordx4 v157, v[134:137], s[36:37] offset:1024 sc1
	s_waitcnt lgkmcnt(0)
	v_lshl_or_b32 v138, v139, 16, v138
	v_lshl_or_b32 v139, v141, 16, v140
	v_lshl_or_b32 v140, v143, 16, v142
	v_lshl_or_b32 v141, v145, 16, v144
	global_store_dwordx4 v157, v[138:141], s[38:39] sc1
	ds_read_u16 v142, v167 offset:4352
	ds_read_u16 v143, v167 offset:4624
	ds_read_u16 v144, v167 offset:4896
	ds_read_u16 v145, v167 offset:5168
	ds_read_u16 v146, v167 offset:5440
	ds_read_u16 v147, v167 offset:5712
	ds_read_u16 v148, v167 offset:5984
	ds_read_u16 v149, v167 offset:6256
	ds_read_b128 v[2:5], v165 offset:0
	ds_read_b128 v[6:9], v165 offset:1056
	ds_read_b128 v[10:13], v165 offset:2112
	ds_read_b128 v[14:17], v165 offset:3168
	s_waitcnt lgkmcnt(4)
	v_lshl_or_b32 v142, v143, 16, v142
	v_lshl_or_b32 v143, v145, 16, v144
	v_lshl_or_b32 v144, v147, 16, v146
	v_lshl_or_b32 v145, v149, 16, v148
	global_store_dwordx4 v157, v[142:145], s[38:39] offset:1024 sc1
	ds_read_b128 v[18:21], v165 offset:4224
	ds_read_b128 v[22:25], v165 offset:5280
	ds_read_b128 v[26:29], v165 offset:6336
	ds_read_b128 v[30:33], v165 offset:7392
	ds_read_b128 v[34:37], v165 offset:8448
	ds_read_b128 v[38:41], v165 offset:9504
	ds_read_b128 v[42:45], v165 offset:10560
	ds_read_b128 v[46:49], v165 offset:11616
	s_waitcnt lgkmcnt(8)
	v_mfma_f32_32x32x16_f16 v[98:113], v[82:85], v[2:5], 0
	v_mfma_f32_32x32x16_f16 v[98:113], v[86:89], v[6:9], v[98:113]
	v_mfma_f32_32x32x16_f16 v[98:113], v[90:93], v[10:13], v[98:113]
	v_mfma_f32_32x32x16_f16 v[98:113], v[94:97], v[14:17], v[98:113]
	ds_read_b128 v[50:53], v165 offset:12672
	ds_read_b128 v[54:57], v165 offset:13728
	ds_read_b128 v[58:61], v165 offset:14784
	ds_read_b128 v[62:65], v165 offset:15840
	s_waitcnt lgkmcnt(8)
	v_mfma_f32_32x32x16_f16 v[114:129], v[82:85], v[18:21], 0
	v_mfma_f32_32x32x16_f16 v[114:129], v[86:89], v[22:25], v[114:129]
	v_mfma_f32_32x32x16_f16 v[114:129], v[90:93], v[26:29], v[114:129]
	v_mfma_f32_32x32x16_f16 v[114:129], v[94:97], v[30:33], v[114:129]
	s_nop 7
	v_pk_fma_f32 v[130:131], v[98:99], s[4:5], v[66:67] op_sel_hi:[1,0,1]
	v_pk_fma_f32 v[132:133], v[100:101], s[4:5], v[68:69] op_sel_hi:[1,0,1]
	v_pk_fma_f32 v[134:135], v[102:103], s[4:5], v[70:71] op_sel_hi:[1,0,1]
	v_pk_fma_f32 v[136:137], v[104:105], s[4:5], v[72:73] op_sel_hi:[1,0,1]
	v_pk_fma_f32 v[138:139], v[106:107], s[4:5], v[74:75] op_sel_hi:[1,0,1]
	v_pk_fma_f32 v[140:141], v[108:109], s[4:5], v[76:77] op_sel_hi:[1,0,1]
	v_pk_fma_f32 v[142:143], v[110:111], s[4:5], v[78:79] op_sel_hi:[1,0,1]
	v_pk_fma_f32 v[144:145], v[112:113], s[4:5], v[80:81] op_sel_hi:[1,0,1]
	v_exp_f32_e32 v130, v130
	v_exp_f32_e32 v131, v131
	v_exp_f32_e32 v132, v132
	v_exp_f32_e32 v133, v133
	v_exp_f32_e32 v134, v134
	v_exp_f32_e32 v135, v135
	v_exp_f32_e32 v136, v136
	v_exp_f32_e32 v137, v137
	v_exp_f32_e32 v138, v138
	v_exp_f32_e32 v139, v139
	v_exp_f32_e32 v140, v140
	v_exp_f32_e32 v141, v141
	v_exp_f32_e32 v142, v142
	v_exp_f32_e32 v143, v143
	v_exp_f32_e32 v144, v144
	v_exp_f32_e32 v145, v145
	v_pk_add_f32 v[130:131], v[130:131], 1.0 op_sel_hi:[1,0]
	v_pk_add_f32 v[132:133], v[132:133], 1.0 op_sel_hi:[1,0]
	v_pk_add_f32 v[134:135], v[134:135], 1.0 op_sel_hi:[1,0]
	v_pk_add_f32 v[136:137], v[136:137], 1.0 op_sel_hi:[1,0]
	v_pk_add_f32 v[138:139], v[138:139], 1.0 op_sel_hi:[1,0]
	v_pk_add_f32 v[140:141], v[140:141], 1.0 op_sel_hi:[1,0]
	v_pk_add_f32 v[142:143], v[142:143], 1.0 op_sel_hi:[1,0]
	v_pk_add_f32 v[144:145], v[144:145], 1.0 op_sel_hi:[1,0]
	v_rcp_f32_e32 v130, v130
	v_rcp_f32_e32 v131, v131
	v_rcp_f32_e32 v132, v132
	v_rcp_f32_e32 v133, v133
	v_rcp_f32_e32 v134, v134
	v_rcp_f32_e32 v135, v135
	v_rcp_f32_e32 v136, v136
	v_rcp_f32_e32 v137, v137
	v_rcp_f32_e32 v138, v138
	v_rcp_f32_e32 v139, v139
	v_rcp_f32_e32 v140, v140
	v_rcp_f32_e32 v141, v141
	v_rcp_f32_e32 v142, v142
	v_rcp_f32_e32 v143, v143
	v_rcp_f32_e32 v144, v144
	v_rcp_f32_e32 v145, v145
	v_pk_fma_f32 v[130:131], v[130:131], 2.0, 1.0 op_sel_hi:[1,0,0] neg_lo:[1,0,0] neg_hi:[1,0,0]
	v_pk_fma_f32 v[132:133], v[132:133], 2.0, 1.0 op_sel_hi:[1,0,0] neg_lo:[1,0,0] neg_hi:[1,0,0]
	v_pk_fma_f32 v[134:135], v[134:135], 2.0, 1.0 op_sel_hi:[1,0,0] neg_lo:[1,0,0] neg_hi:[1,0,0]
	v_pk_fma_f32 v[136:137], v[136:137], 2.0, 1.0 op_sel_hi:[1,0,0] neg_lo:[1,0,0] neg_hi:[1,0,0]
	v_pk_fma_f32 v[138:139], v[138:139], 2.0, 1.0 op_sel_hi:[1,0,0] neg_lo:[1,0,0] neg_hi:[1,0,0]
	v_pk_fma_f32 v[140:141], v[140:141], 2.0, 1.0 op_sel_hi:[1,0,0] neg_lo:[1,0,0] neg_hi:[1,0,0]
	v_pk_fma_f32 v[142:143], v[142:143], 2.0, 1.0 op_sel_hi:[1,0,0] neg_lo:[1,0,0] neg_hi:[1,0,0]
	v_pk_fma_f32 v[144:145], v[144:145], 2.0, 1.0 op_sel_hi:[1,0,0] neg_lo:[1,0,0] neg_hi:[1,0,0]
	v_cvt_pk_f16_f32 v146, v130, v131
	v_cvt_pk_f16_f32 v147, v132, v133
	v_cvt_pk_f16_f32 v148, v134, v135
	v_cvt_pk_f16_f32 v149, v136, v137
	v_cvt_pk_f16_f32 v150, v138, v139
	v_cvt_pk_f16_f32 v151, v140, v141
	v_cvt_pk_f16_f32 v152, v142, v143
	v_cvt_pk_f16_f32 v153, v144, v145
	s_nop 1
	v_permlane32_swap_b32_e32 v146, v148
	v_permlane32_swap_b32_e32 v147, v149
	v_permlane32_swap_b32_e32 v150, v152
	v_permlane32_swap_b32_e32 v151, v153
	global_store_dwordx4 v157, v[146:149], s[32:33] sc1
	global_store_dwordx4 v157, v[150:153], s[32:33] offset:1024 sc1
	s_add_u32 s32, s32, 0x10000
	s_addc_u32 s33, s33, 0
	s_waitcnt lgkmcnt(4)
	v_mfma_f32_32x32x16_f16 v[98:113], v[82:85], v[34:37], 0
	v_mfma_f32_32x32x16_f16 v[98:113], v[86:89], v[38:41], v[98:113]
	v_mfma_f32_32x32x16_f16 v[98:113], v[90:93], v[42:45], v[98:113]
	v_mfma_f32_32x32x16_f16 v[98:113], v[94:97], v[46:49], v[98:113]
	v_pk_fma_f32 v[130:131], v[114:115], s[4:5], v[66:67] op_sel_hi:[1,0,1]
	v_pk_fma_f32 v[132:133], v[116:117], s[4:5], v[68:69] op_sel_hi:[1,0,1]
	v_pk_fma_f32 v[134:135], v[118:119], s[4:5], v[70:71] op_sel_hi:[1,0,1]
	v_pk_fma_f32 v[136:137], v[120:121], s[4:5], v[72:73] op_sel_hi:[1,0,1]
	v_pk_fma_f32 v[138:139], v[122:123], s[4:5], v[74:75] op_sel_hi:[1,0,1]
	v_pk_fma_f32 v[140:141], v[124:125], s[4:5], v[76:77] op_sel_hi:[1,0,1]
	v_pk_fma_f32 v[142:143], v[126:127], s[4:5], v[78:79] op_sel_hi:[1,0,1]
	v_pk_fma_f32 v[144:145], v[128:129], s[4:5], v[80:81] op_sel_hi:[1,0,1]
	v_exp_f32_e32 v130, v130
	v_exp_f32_e32 v131, v131
	v_exp_f32_e32 v132, v132
	v_exp_f32_e32 v133, v133
	v_exp_f32_e32 v134, v134
	v_exp_f32_e32 v135, v135
	v_exp_f32_e32 v136, v136
	v_exp_f32_e32 v137, v137
	v_exp_f32_e32 v138, v138
	v_exp_f32_e32 v139, v139
	v_exp_f32_e32 v140, v140
	v_exp_f32_e32 v141, v141
	v_exp_f32_e32 v142, v142
	v_exp_f32_e32 v143, v143
	v_exp_f32_e32 v144, v144
	v_exp_f32_e32 v145, v145
	v_pk_add_f32 v[130:131], v[130:131], 1.0 op_sel_hi:[1,0]
	v_pk_add_f32 v[132:133], v[132:133], 1.0 op_sel_hi:[1,0]
	v_pk_add_f32 v[134:135], v[134:135], 1.0 op_sel_hi:[1,0]
	v_pk_add_f32 v[136:137], v[136:137], 1.0 op_sel_hi:[1,0]
	v_pk_add_f32 v[138:139], v[138:139], 1.0 op_sel_hi:[1,0]
	v_pk_add_f32 v[140:141], v[140:141], 1.0 op_sel_hi:[1,0]
	v_pk_add_f32 v[142:143], v[142:143], 1.0 op_sel_hi:[1,0]
	v_pk_add_f32 v[144:145], v[144:145], 1.0 op_sel_hi:[1,0]
	v_rcp_f32_e32 v130, v130
	v_rcp_f32_e32 v131, v131
	v_rcp_f32_e32 v132, v132
	v_rcp_f32_e32 v133, v133
	v_rcp_f32_e32 v134, v134
	v_rcp_f32_e32 v135, v135
	v_rcp_f32_e32 v136, v136
	v_rcp_f32_e32 v137, v137
	v_rcp_f32_e32 v138, v138
	v_rcp_f32_e32 v139, v139
	v_rcp_f32_e32 v140, v140
	v_rcp_f32_e32 v141, v141
	v_rcp_f32_e32 v142, v142
	v_rcp_f32_e32 v143, v143
	v_rcp_f32_e32 v144, v144
	v_rcp_f32_e32 v145, v145
	v_pk_fma_f32 v[130:131], v[130:131], 2.0, 1.0 op_sel_hi:[1,0,0] neg_lo:[1,0,0] neg_hi:[1,0,0]
	v_pk_fma_f32 v[132:133], v[132:133], 2.0, 1.0 op_sel_hi:[1,0,0] neg_lo:[1,0,0] neg_hi:[1,0,0]
	v_pk_fma_f32 v[134:135], v[134:135], 2.0, 1.0 op_sel_hi:[1,0,0] neg_lo:[1,0,0] neg_hi:[1,0,0]
	v_pk_fma_f32 v[136:137], v[136:137], 2.0, 1.0 op_sel_hi:[1,0,0] neg_lo:[1,0,0] neg_hi:[1,0,0]
	v_pk_fma_f32 v[138:139], v[138:139], 2.0, 1.0 op_sel_hi:[1,0,0] neg_lo:[1,0,0] neg_hi:[1,0,0]
	v_pk_fma_f32 v[140:141], v[140:141], 2.0, 1.0 op_sel_hi:[1,0,0] neg_lo:[1,0,0] neg_hi:[1,0,0]
	v_pk_fma_f32 v[142:143], v[142:143], 2.0, 1.0 op_sel_hi:[1,0,0] neg_lo:[1,0,0] neg_hi:[1,0,0]
	v_pk_fma_f32 v[144:145], v[144:145], 2.0, 1.0 op_sel_hi:[1,0,0] neg_lo:[1,0,0] neg_hi:[1,0,0]
	v_cvt_pk_f16_f32 v146, v130, v131
	v_cvt_pk_f16_f32 v147, v132, v133
	v_cvt_pk_f16_f32 v148, v134, v135
	v_cvt_pk_f16_f32 v149, v136, v137
	v_cvt_pk_f16_f32 v150, v138, v139
	v_cvt_pk_f16_f32 v151, v140, v141
	v_cvt_pk_f16_f32 v152, v142, v143
	v_cvt_pk_f16_f32 v153, v144, v145
	s_nop 1
	v_permlane32_swap_b32_e32 v146, v148
	v_permlane32_swap_b32_e32 v147, v149
	v_permlane32_swap_b32_e32 v150, v152
	v_permlane32_swap_b32_e32 v151, v153
	global_store_dwordx4 v157, v[146:149], s[32:33] sc1
	global_store_dwordx4 v157, v[150:153], s[32:33] offset:1024 sc1
	s_add_u32 s32, s32, 0x10000
	s_addc_u32 s33, s33, 0
	s_waitcnt lgkmcnt(0)
	v_mfma_f32_32x32x16_f16 v[114:129], v[82:85], v[50:53], 0
	v_mfma_f32_32x32x16_f16 v[114:129], v[86:89], v[54:57], v[114:129]
	v_mfma_f32_32x32x16_f16 v[114:129], v[90:93], v[58:61], v[114:129]
	v_mfma_f32_32x32x16_f16 v[114:129], v[94:97], v[62:65], v[114:129]
	v_pk_fma_f32 v[130:131], v[98:99], s[4:5], v[66:67] op_sel_hi:[1,0,1]
	v_pk_fma_f32 v[132:133], v[100:101], s[4:5], v[68:69] op_sel_hi:[1,0,1]
	v_pk_fma_f32 v[134:135], v[102:103], s[4:5], v[70:71] op_sel_hi:[1,0,1]
	v_pk_fma_f32 v[136:137], v[104:105], s[4:5], v[72:73] op_sel_hi:[1,0,1]
	v_pk_fma_f32 v[138:139], v[106:107], s[4:5], v[74:75] op_sel_hi:[1,0,1]
	v_pk_fma_f32 v[140:141], v[108:109], s[4:5], v[76:77] op_sel_hi:[1,0,1]
	v_pk_fma_f32 v[142:143], v[110:111], s[4:5], v[78:79] op_sel_hi:[1,0,1]
	v_pk_fma_f32 v[144:145], v[112:113], s[4:5], v[80:81] op_sel_hi:[1,0,1]
	v_exp_f32_e32 v130, v130
	v_exp_f32_e32 v131, v131
	v_exp_f32_e32 v132, v132
	v_exp_f32_e32 v133, v133
	v_exp_f32_e32 v134, v134
	v_exp_f32_e32 v135, v135
	v_exp_f32_e32 v136, v136
	v_exp_f32_e32 v137, v137
	v_exp_f32_e32 v138, v138
	v_exp_f32_e32 v139, v139
	v_exp_f32_e32 v140, v140
	v_exp_f32_e32 v141, v141
	v_exp_f32_e32 v142, v142
	v_exp_f32_e32 v143, v143
	v_exp_f32_e32 v144, v144
	v_exp_f32_e32 v145, v145
	v_pk_add_f32 v[130:131], v[130:131], 1.0 op_sel_hi:[1,0]
	v_pk_add_f32 v[132:133], v[132:133], 1.0 op_sel_hi:[1,0]
	v_pk_add_f32 v[134:135], v[134:135], 1.0 op_sel_hi:[1,0]
	v_pk_add_f32 v[136:137], v[136:137], 1.0 op_sel_hi:[1,0]
	v_pk_add_f32 v[138:139], v[138:139], 1.0 op_sel_hi:[1,0]
	v_pk_add_f32 v[140:141], v[140:141], 1.0 op_sel_hi:[1,0]
	v_pk_add_f32 v[142:143], v[142:143], 1.0 op_sel_hi:[1,0]
	v_pk_add_f32 v[144:145], v[144:145], 1.0 op_sel_hi:[1,0]
	v_rcp_f32_e32 v130, v130
	v_rcp_f32_e32 v131, v131
	v_rcp_f32_e32 v132, v132
	v_rcp_f32_e32 v133, v133
	v_rcp_f32_e32 v134, v134
	v_rcp_f32_e32 v135, v135
	v_rcp_f32_e32 v136, v136
	v_rcp_f32_e32 v137, v137
	v_rcp_f32_e32 v138, v138
	v_rcp_f32_e32 v139, v139
	v_rcp_f32_e32 v140, v140
	v_rcp_f32_e32 v141, v141
	v_rcp_f32_e32 v142, v142
	v_rcp_f32_e32 v143, v143
	v_rcp_f32_e32 v144, v144
	v_rcp_f32_e32 v145, v145
	v_pk_fma_f32 v[130:131], v[130:131], 2.0, 1.0 op_sel_hi:[1,0,0] neg_lo:[1,0,0] neg_hi:[1,0,0]
	v_pk_fma_f32 v[132:133], v[132:133], 2.0, 1.0 op_sel_hi:[1,0,0] neg_lo:[1,0,0] neg_hi:[1,0,0]
	v_pk_fma_f32 v[134:135], v[134:135], 2.0, 1.0 op_sel_hi:[1,0,0] neg_lo:[1,0,0] neg_hi:[1,0,0]
	v_pk_fma_f32 v[136:137], v[136:137], 2.0, 1.0 op_sel_hi:[1,0,0] neg_lo:[1,0,0] neg_hi:[1,0,0]
	v_pk_fma_f32 v[138:139], v[138:139], 2.0, 1.0 op_sel_hi:[1,0,0] neg_lo:[1,0,0] neg_hi:[1,0,0]
	v_pk_fma_f32 v[140:141], v[140:141], 2.0, 1.0 op_sel_hi:[1,0,0] neg_lo:[1,0,0] neg_hi:[1,0,0]
	v_pk_fma_f32 v[142:143], v[142:143], 2.0, 1.0 op_sel_hi:[1,0,0] neg_lo:[1,0,0] neg_hi:[1,0,0]
	v_pk_fma_f32 v[144:145], v[144:145], 2.0, 1.0 op_sel_hi:[1,0,0] neg_lo:[1,0,0] neg_hi:[1,0,0]
	v_cvt_pk_f16_f32 v146, v130, v131
	v_cvt_pk_f16_f32 v147, v132, v133
	v_cvt_pk_f16_f32 v148, v134, v135
	v_cvt_pk_f16_f32 v149, v136, v137
	v_cvt_pk_f16_f32 v150, v138, v139
	v_cvt_pk_f16_f32 v151, v140, v141
	v_cvt_pk_f16_f32 v152, v142, v143
	v_cvt_pk_f16_f32 v153, v144, v145
	s_nop 1
	v_permlane32_swap_b32_e32 v146, v148
	v_permlane32_swap_b32_e32 v147, v149
	v_permlane32_swap_b32_e32 v150, v152
	v_permlane32_swap_b32_e32 v151, v153
	global_store_dwordx4 v157, v[146:149], s[32:33] sc1
	global_store_dwordx4 v157, v[150:153], s[32:33] offset:1024 sc1
	s_add_u32 s32, s32, 0x10000
	s_addc_u32 s33, s33, 0
	s_nop 7
	v_pk_fma_f32 v[130:131], v[114:115], s[4:5], v[66:67] op_sel_hi:[1,0,1]
	v_pk_fma_f32 v[132:133], v[116:117], s[4:5], v[68:69] op_sel_hi:[1,0,1]
	v_pk_fma_f32 v[134:135], v[118:119], s[4:5], v[70:71] op_sel_hi:[1,0,1]
	v_pk_fma_f32 v[136:137], v[120:121], s[4:5], v[72:73] op_sel_hi:[1,0,1]
	v_pk_fma_f32 v[138:139], v[122:123], s[4:5], v[74:75] op_sel_hi:[1,0,1]
	v_pk_fma_f32 v[140:141], v[124:125], s[4:5], v[76:77] op_sel_hi:[1,0,1]
	v_pk_fma_f32 v[142:143], v[126:127], s[4:5], v[78:79] op_sel_hi:[1,0,1]
	v_pk_fma_f32 v[144:145], v[128:129], s[4:5], v[80:81] op_sel_hi:[1,0,1]
	v_exp_f32_e32 v130, v130
	v_exp_f32_e32 v131, v131
	v_exp_f32_e32 v132, v132
	v_exp_f32_e32 v133, v133
	v_exp_f32_e32 v134, v134
	v_exp_f32_e32 v135, v135
	v_exp_f32_e32 v136, v136
	v_exp_f32_e32 v137, v137
	v_exp_f32_e32 v138, v138
	v_exp_f32_e32 v139, v139
	v_exp_f32_e32 v140, v140
	v_exp_f32_e32 v141, v141
	v_exp_f32_e32 v142, v142
	v_exp_f32_e32 v143, v143
	v_exp_f32_e32 v144, v144
	v_exp_f32_e32 v145, v145
	v_pk_add_f32 v[130:131], v[130:131], 1.0 op_sel_hi:[1,0]
	v_pk_add_f32 v[132:133], v[132:133], 1.0 op_sel_hi:[1,0]
	v_pk_add_f32 v[134:135], v[134:135], 1.0 op_sel_hi:[1,0]
	v_pk_add_f32 v[136:137], v[136:137], 1.0 op_sel_hi:[1,0]
	v_pk_add_f32 v[138:139], v[138:139], 1.0 op_sel_hi:[1,0]
	v_pk_add_f32 v[140:141], v[140:141], 1.0 op_sel_hi:[1,0]
	v_pk_add_f32 v[142:143], v[142:143], 1.0 op_sel_hi:[1,0]
	v_pk_add_f32 v[144:145], v[144:145], 1.0 op_sel_hi:[1,0]
	v_rcp_f32_e32 v130, v130
	v_rcp_f32_e32 v131, v131
	v_rcp_f32_e32 v132, v132
	v_rcp_f32_e32 v133, v133
	v_rcp_f32_e32 v134, v134
	v_rcp_f32_e32 v135, v135
	v_rcp_f32_e32 v136, v136
	v_rcp_f32_e32 v137, v137
	v_rcp_f32_e32 v138, v138
	v_rcp_f32_e32 v139, v139
	v_rcp_f32_e32 v140, v140
	v_rcp_f32_e32 v141, v141
	v_rcp_f32_e32 v142, v142
	v_rcp_f32_e32 v143, v143
	v_rcp_f32_e32 v144, v144
	v_rcp_f32_e32 v145, v145
	v_pk_fma_f32 v[130:131], v[130:131], 2.0, 1.0 op_sel_hi:[1,0,0] neg_lo:[1,0,0] neg_hi:[1,0,0]
	v_pk_fma_f32 v[132:133], v[132:133], 2.0, 1.0 op_sel_hi:[1,0,0] neg_lo:[1,0,0] neg_hi:[1,0,0]
	v_pk_fma_f32 v[134:135], v[134:135], 2.0, 1.0 op_sel_hi:[1,0,0] neg_lo:[1,0,0] neg_hi:[1,0,0]
	v_pk_fma_f32 v[136:137], v[136:137], 2.0, 1.0 op_sel_hi:[1,0,0] neg_lo:[1,0,0] neg_hi:[1,0,0]
	v_pk_fma_f32 v[138:139], v[138:139], 2.0, 1.0 op_sel_hi:[1,0,0] neg_lo:[1,0,0] neg_hi:[1,0,0]
	v_pk_fma_f32 v[140:141], v[140:141], 2.0, 1.0 op_sel_hi:[1,0,0] neg_lo:[1,0,0] neg_hi:[1,0,0]
	v_pk_fma_f32 v[142:143], v[142:143], 2.0, 1.0 op_sel_hi:[1,0,0] neg_lo:[1,0,0] neg_hi:[1,0,0]
	v_pk_fma_f32 v[144:145], v[144:145], 2.0, 1.0 op_sel_hi:[1,0,0] neg_lo:[1,0,0] neg_hi:[1,0,0]
	v_cvt_pk_f16_f32 v146, v130, v131
	v_cvt_pk_f16_f32 v147, v132, v133
	v_cvt_pk_f16_f32 v148, v134, v135
	v_cvt_pk_f16_f32 v149, v136, v137
	v_cvt_pk_f16_f32 v150, v138, v139
	v_cvt_pk_f16_f32 v151, v140, v141
	v_cvt_pk_f16_f32 v152, v142, v143
	v_cvt_pk_f16_f32 v153, v144, v145
	s_nop 1
	v_permlane32_swap_b32_e32 v146, v148
	v_permlane32_swap_b32_e32 v147, v149
	v_permlane32_swap_b32_e32 v150, v152
	v_permlane32_swap_b32_e32 v151, v153
	global_store_dwordx4 v157, v[146:149], s[32:33] sc1
	global_store_dwordx4 v157, v[150:153], s[32:33] offset:1024 sc1
	s_endpgm
